# v39 + indexer bitmask-word stores issued one unit later (after the next scoring barrier) so their acks are off the in-order vmcnt waits
# baseline (speedup 1.0000x reference)
.LBB0_1222:
	v_readlane_b32 s0, v253, 38
	s_lshl_b32 s80, s0, 6
	s_lshl_b64 s[0:1], s[80:81], 2
	s_add_u32 s0, s74, s0
	s_addc_u32 s1, s75, s1
	s_add_u32 s0, s0, 0x1000
	s_addc_u32 s1, s1, 0
	v_writelane_b32 v253, s0, 53
	s_mov_b32 s101, -1
	s_waitcnt vmcnt(0) lgkmcnt(0)
	s_barrier
	v_writelane_b32 v253, s1, 54
	s_nop 0
	v_readlane_b32 s0, v253, 32
	v_readlane_b32 s1, v253, 33
	s_nop 0
	v_or_b32_e32 v0, s0, v198
	v_cmp_eq_u32_e64 s[36:37], 0, v0
	s_and_saveexec_b64 s[0:1], s[36:37]
	s_cbranch_execz .LBB0_1226
	s_mov_b64 s[16:17], exec
	v_mbcnt_lo_u32_b32 v0, s16, 0
	v_mbcnt_hi_u32_b32 v0, s17, v0
	v_cmp_eq_u32_e32 vcc, 0, v0
	s_and_saveexec_b64 s[14:15], vcc
	s_cbranch_execz .LBB0_1225
	s_bcnt1_i32_b64 s16, s[16:17]
	v_mov_b32_e32 v2, s16
	v_readlane_b32 s16, v253, 53
	v_readlane_b32 s17, v253, 54
	s_nop 4
	global_atomic_add v2, v1, v2, s[16:17] sc0

.LBB0_1252:
	s_or_b64 exec, exec, s[40:41]
	s_lshl_b32 s17, s17, 2
	s_or_b32 s17, s17, 0x20420
	s_waitcnt lgkmcnt(0)
	s_barrier
	s_cmp_lt_i32 s101, 0
	s_cbranch_scc1 .Lbm_none_a
	v_cmp_ge_i32_e64 s[44:45], s101, v104
	s_and_saveexec_b64 s[42:43], s[44:45]
	global_store_dword v[160:161], v162, off
	s_or_b64 exec, exec, s[42:43]
	v_cmp_ge_i32_e64 s[44:45], s101, v105
	s_and_saveexec_b64 s[42:43], s[44:45]
	global_store_dword v[164:165], v163, off
	s_or_b64 exec, exec, s[42:43]
	s_mov_b32 s101, -1
.Lbm_none_a:
	v_mov_b32_e32 v0, s17
	ds_read_b32 v0, v0
	s_movk_i32 s29, 0xfff
	s_waitcnt lgkmcnt(0)
	v_cmp_lt_u32_e64 s[40:41], s29, v0
	v_readfirstlane_b32 s17, v0
	s_and_b64 vcc, exec, s[40:41]
	s_cbranch_vccnz .LBB0_1256
	s_not_b32 s29, s17
	s_lshl_b32 s29, s29, 1
	s_lshl_b32 s43, s17, 13
	s_and_b32 s42, s29, 0x1ffc
	s_and_b32 s43, s43, 0x2000
	s_or_b32 s42, s42, s43
	v_or_b32_e32 v0, s42, v143
	v_lshlrev_b32_e32 v0, 10, v0
	s_bfe_u32 s29, s29, 0x80005
	v_readlane_b32 s44, v253, 32
	v_lshl_add_u64 v[2:3], v[102:103], 0, v[0:1]
	v_or_b32_e32 v0, s42, v140
	s_min_i32 s42, s44, s29
	v_readlane_b32 s44, v253, 31
	s_min_i32 s29, s44, s29
	s_lshr_b32 s44, s43, 5
	s_ashr_i32 s43, s42, 31
	s_add_u32 s42, s42, s44
	s_addc_u32 s43, s43, 0
	s_lshl_b64 s[42:43], s[42:43], 12
	global_load_dwordx4 v[18:21], v[2:3], off
	global_load_dwordx4 v[26:29], v[2:3], off offset:32
	global_load_dwordx4 v[30:33], v[2:3], off offset:64
	global_load_dwordx4 v[34:37], v[2:3], off offset:96
	v_lshl_add_u64 v[2:3], v[100:101], 0, s[42:43]
	s_ashr_i32 s43, s29, 31
	s_add_u32 s42, s29, s44
	s_addc_u32 s43, s43, 0
	v_lshlrev_b32_e32 v0, 5, v0
	s_lshl_b64 s[42:43], s[42:43], 12
	global_load_dwordx4 v[22:25], v0, s[82:83]
	global_load_dwordx4 v[38:41], v0, s[82:83] offset:16
	global_load_dwordx4 v[42:45], v0, s[82:83] offset:64
	global_load_dwordx4 v[46:49], v0, s[82:83] offset:80
	v_lshl_add_u64 v[4:5], v[100:101], 0, s[42:43]
	global_load_dwordx4 v[50:53], v[2:3], off
	global_load_dwordx4 v[62:65], v[2:3], off offset:1024
	global_load_dwordx4 v[78:81], v[4:5], off
	global_load_dwordx4 v[70:73], v[4:5], off offset:1024
	global_load_dwordx4 v[58:61], v[2:3], off offset:2048
	global_load_dwordx4 v[54:57], v[2:3], off offset:3072
	global_load_dwordx4 v[74:77], v[4:5], off offset:2048
	global_load_dwordx4 v[66:69], v[4:5], off offset:3072
	v_readlane_b32 s45, v253, 33
	s_cmpk_lt_u32 s34, 0x100
	v_mov_b32_e32 v149, 1
	s_cbranch_scc0 .LBB0_1257

.LBB0_1975:
	s_lshl_b32 s80, s0, 23
	v_lshl_add_u64 v[2:3], v[106:107], 0, s[80:81]
	s_lshl_b32 s80, s34, 2
	s_or_b32 s29, s1, 7
	v_lshl_add_u64 v[2:3], v[2:3], 0, s[80:81]
	s_mov_b32 s65, s81
	v_readlane_b32 s91, v253, 27
	v_readlane_b32 s92, v253, 28
	s_mov_b32 s89, 0x2e8ba2e9
	s_movk_i32 s95, 0x100
	s_movk_i32 s90, 0xfea0
	s_movk_i32 s94, 0x2000
	v_lshl_add_u64 v[2:3], v[2:3], 0, s[64:65]
	v_mov_b32_e32 v160, v2
	v_mov_b32_e32 v161, v3
	v_mov_b32_e32 v162, v0
	v_mov_b32_e32 v163, v4
	v_add_co_u32_e32 v164, vcc, 0x400000, v2
	s_nop 1
	v_addc_co_u32_e32 v165, vcc, 0, v3, vcc
	s_mov_b32 s101, s29
	v_cmp_ge_i32_e32 vcc, s29, v104
	v_readlane_b32 s93, v253, 29
	s_and_saveexec_b64 s[42:43], vcc
	s_cbranch_execz .LBB0_1977
.LBB0_1977:
	s_or_b64 exec, exec, s[42:43]
	v_cmp_ge_i32_e32 vcc, s29, v105
	s_and_saveexec_b64 s[42:43], vcc
	s_cbranch_execz .LBB0_1979
	v_add_co_u32_e32 v2, vcc, 0x400000, v2
	s_nop 1
	v_addc_co_u32_e32 v3, vcc, 0, v3, vcc
.LBB0_1979:
	s_or_b64 exec, exec, s[42:43]
	s_and_saveexec_b64 s[42:43], s[14:15]
	s_cbranch_execnz .LBB0_1255

.LBB0_1988:
	s_cmp_lt_i32 s101, 0
	s_cbranch_scc1 .Lbm_none_b
	v_cmp_ge_i32_e64 s[44:45], s101, v104
	s_and_saveexec_b64 s[42:43], s[44:45]
	global_store_dword v[160:161], v162, off
	s_or_b64 exec, exec, s[42:43]
	v_cmp_ge_i32_e64 s[44:45], s101, v105
	s_and_saveexec_b64 s[42:43], s[44:45]
	global_store_dword v[164:165], v163, off
	s_or_b64 exec, exec, s[42:43]
	s_mov_b32 s101, -1
